# speedup vs baseline: 1.0086x; 1.0086x over previous
.LBB1_82:
	ds_read_b128 v[130:133], v219 offset:32768
	ds_read_b128 v[134:137], v219 offset:33792
	ds_read_b128 v[138:141], v219 offset:34816
	ds_read_b128 v[142:145], v219 offset:35840
	ds_read_b128 v[146:149], v220
	ds_read_b128 v[150:153], v220 offset:1024
	ds_read_b128 v[154:157], v221
	ds_read_b128 v[158:161], v221 offset:1024
	ds_read_b128 v[162:165], v222
	ds_read_b128 v[166:169], v222 offset:1024
	ds_read_b128 v[170:173], v223
	ds_read_b128 v[174:177], v223 offset:1024
	s_setprio 2
	s_add_i32 s12, s8, 1
	v_readlane_b32 s9, v248, s12
	s_mov_b32 m0, s43
	s_nop 1
	v_add_u32_e32 v129, s9, v249
	global_load_lds_dwordx4 v129, s[18:19]
	v_add_u32_e32 v129, s9, v250
	s_mov_b32 m0, s44
	s_nop 0
	global_load_lds_dwordx4 v129, s[18:19]
	s_setprio 0
	s_waitcnt vmcnt(10)
	s_waitcnt lgkmcnt(8)
	s_barrier
	s_waitcnt lgkmcnt(0)
	s_setprio 1
	s_waitcnt lgkmcnt(0)
	v_mfma_f32_16x16x32_f16 v[124:127], v[130:133], v[146:149], v[124:127]
	v_mfma_f32_16x16x32_f16 v[120:123], v[138:141], v[146:149], v[120:123]
	v_mfma_f32_16x16x32_f16 v[116:119], v[130:133], v[154:157], v[116:119]
	v_mfma_f32_16x16x32_f16 v[112:115], v[138:141], v[154:157], v[112:115]
	v_mfma_f32_16x16x32_f16 v[108:111], v[130:133], v[162:165], v[108:111]
	v_mfma_f32_16x16x32_f16 v[104:107], v[138:141], v[162:165], v[104:107]
	v_mfma_f32_16x16x32_f16 v[100:103], v[130:133], v[170:173], v[100:103]
	v_mfma_f32_16x16x32_f16 v[96:99], v[138:141], v[170:173], v[96:99]
	v_mfma_f32_16x16x32_f16 v[124:127], v[134:137], v[150:153], v[124:127]
	v_mfma_f32_16x16x32_f16 v[120:123], v[142:145], v[150:153], v[120:123]
	v_mfma_f32_16x16x32_f16 v[116:119], v[134:137], v[158:161], v[116:119]
	v_mfma_f32_16x16x32_f16 v[112:115], v[142:145], v[158:161], v[112:115]
	v_mfma_f32_16x16x32_f16 v[108:111], v[134:137], v[166:169], v[108:111]
	v_mfma_f32_16x16x32_f16 v[104:107], v[142:145], v[166:169], v[104:107]
	v_mfma_f32_16x16x32_f16 v[100:103], v[134:137], v[174:177], v[100:103]
	v_mfma_f32_16x16x32_f16 v[96:99], v[142:145], v[174:177], v[96:99]
	s_setprio 0
	s_barrier
	ds_read_b128 v[178:181], v219 offset:49152
	ds_read_b128 v[182:185], v219 offset:50176
	ds_read_b128 v[186:189], v219 offset:51200
	ds_read_b128 v[190:193], v219 offset:52224
	s_setprio 2
	v_add_u32_e32 v129, s7, v128
	s_mov_b32 m0, s22
	v_add_u32_e32 v194, 0xffffff80, v129
	global_load_lds_dwordx4 v194, s[10:11]
	v_add_u32_e32 v194, 0x47f80, v129
	s_mov_b32 m0, s23
	s_add_i32 s9, s8, 2
	global_load_lds_dwordx4 v194, s[10:11]
	s_setprio 0
	s_waitcnt vmcnt(10)
	s_barrier
	s_waitcnt lgkmcnt(0)
	s_setprio 1
	s_waitcnt lgkmcnt(0)
	v_mfma_f32_16x16x32_f16 v[52:55], v[178:181], v[146:149], v[52:55]
	v_mfma_f32_16x16x32_f16 v[40:43], v[186:189], v[146:149], v[40:43]
	v_mfma_f32_16x16x32_f16 v[36:39], v[178:181], v[154:157], v[36:39]
	v_mfma_f32_16x16x32_f16 v[32:35], v[186:189], v[154:157], v[32:35]
	v_mfma_f32_16x16x32_f16 v[28:31], v[178:181], v[162:165], v[28:31]
	v_mfma_f32_16x16x32_f16 v[24:27], v[186:189], v[162:165], v[24:27]
	v_mfma_f32_16x16x32_f16 v[20:23], v[178:181], v[170:173], v[20:23]
	v_mfma_f32_16x16x32_f16 v[16:19], v[186:189], v[170:173], v[16:19]
	v_mfma_f32_16x16x32_f16 v[52:55], v[182:185], v[150:153], v[52:55]
	v_mfma_f32_16x16x32_f16 v[40:43], v[190:193], v[150:153], v[40:43]
	v_mfma_f32_16x16x32_f16 v[36:39], v[182:185], v[158:161], v[36:39]
	v_mfma_f32_16x16x32_f16 v[32:35], v[190:193], v[158:161], v[32:35]
	v_mfma_f32_16x16x32_f16 v[28:31], v[182:185], v[166:169], v[28:31]
	v_mfma_f32_16x16x32_f16 v[24:27], v[190:193], v[166:169], v[24:27]
	v_mfma_f32_16x16x32_f16 v[20:23], v[182:185], v[174:177], v[20:23]
	v_mfma_f32_16x16x32_f16 v[16:19], v[190:193], v[174:177], v[16:19]
	s_setprio 0
	s_barrier
	ds_read_b128 v[146:149], v220 offset:16384
	ds_read_b128 v[150:153], v220 offset:17408
	ds_read_b128 v[154:157], v221 offset:16384
	ds_read_b128 v[158:161], v221 offset:17408
	ds_read_b128 v[162:165], v222 offset:16384
	ds_read_b128 v[166:169], v222 offset:17408
	ds_read_b128 v[170:173], v223 offset:16384
	ds_read_b128 v[174:177], v223 offset:17408
	s_setprio 2
	v_readlane_b32 s13, v248, s9
	s_mov_b32 m0, s21
	s_nop 1
	v_add_u32_e32 v194, s13, v206
	global_load_lds_dwordx4 v194, s[18:19]
	v_add_u32_e32 v194, s13, v213
	s_mov_b32 m0, s24
	s_nop 0
	global_load_lds_dwordx4 v194, s[18:19]
	s_setprio 0
	s_barrier
	s_waitcnt lgkmcnt(0)
	s_setprio 1
	s_waitcnt lgkmcnt(0)
	v_mfma_f32_16x16x32_f16 v[12:15], v[130:133], v[146:149], v[12:15]
	v_mfma_f32_16x16x32_f16 v[8:11], v[138:141], v[146:149], v[8:11]
	v_mfma_f32_16x16x32_f16 v[4:7], v[130:133], v[154:157], v[4:7]
	v_mfma_f32_16x16x32_f16 v[0:3], v[138:141], v[154:157], v[0:3]
	v_mfma_f32_16x16x32_f16 v[44:47], v[130:133], v[162:165], v[44:47]
	v_mfma_f32_16x16x32_f16 v[48:51], v[138:141], v[162:165], v[48:51]
	v_mfma_f32_16x16x32_f16 v[56:59], v[130:133], v[170:173], v[56:59]
	v_mfma_f32_16x16x32_f16 v[60:63], v[138:141], v[170:173], v[60:63]
	v_mfma_f32_16x16x32_f16 v[12:15], v[134:137], v[150:153], v[12:15]
	v_mfma_f32_16x16x32_f16 v[8:11], v[142:145], v[150:153], v[8:11]
	v_mfma_f32_16x16x32_f16 v[4:7], v[134:137], v[158:161], v[4:7]
	v_mfma_f32_16x16x32_f16 v[0:3], v[142:145], v[158:161], v[0:3]
	v_mfma_f32_16x16x32_f16 v[44:47], v[134:137], v[166:169], v[44:47]
	v_mfma_f32_16x16x32_f16 v[48:51], v[142:145], v[166:169], v[48:51]
	v_mfma_f32_16x16x32_f16 v[56:59], v[134:137], v[174:177], v[56:59]
	v_mfma_f32_16x16x32_f16 v[60:63], v[142:145], v[174:177], v[60:63]
	s_setprio 0
	s_barrier
	s_setprio 2
	s_mov_b32 m0, s25
	v_add_u32_e32 v130, 0x8ff80, v129
	global_load_lds_dwordx4 v130, s[10:11]
	v_add_u32_e32 v130, 0xd7f80, v129
	s_mov_b32 m0, s26
	s_nop 0
	global_load_lds_dwordx4 v130, s[10:11]
	s_setprio 0
	s_waitcnt vmcnt(10)
	s_barrier
	s_setprio 1
	v_mfma_f32_16x16x32_f16 v[64:67], v[178:181], v[146:149], v[64:67]
	v_mfma_f32_16x16x32_f16 v[68:71], v[186:189], v[146:149], v[68:71]
	v_mfma_f32_16x16x32_f16 v[72:75], v[178:181], v[154:157], v[72:75]
	v_mfma_f32_16x16x32_f16 v[76:79], v[186:189], v[154:157], v[76:79]
	v_mfma_f32_16x16x32_f16 v[80:83], v[178:181], v[162:165], v[80:83]
	v_mfma_f32_16x16x32_f16 v[84:87], v[186:189], v[162:165], v[84:87]
	v_mfma_f32_16x16x32_f16 v[88:91], v[178:181], v[170:173], v[88:91]
	v_mfma_f32_16x16x32_f16 v[92:95], v[186:189], v[170:173], v[92:95]
	v_mfma_f32_16x16x32_f16 v[64:67], v[182:185], v[150:153], v[64:67]
	v_mfma_f32_16x16x32_f16 v[68:71], v[190:193], v[150:153], v[68:71]
	v_mfma_f32_16x16x32_f16 v[72:75], v[182:185], v[158:161], v[72:75]
	v_mfma_f32_16x16x32_f16 v[76:79], v[190:193], v[158:161], v[76:79]
	v_mfma_f32_16x16x32_f16 v[80:83], v[182:185], v[166:169], v[80:83]
	v_mfma_f32_16x16x32_f16 v[84:87], v[190:193], v[166:169], v[84:87]
	v_mfma_f32_16x16x32_f16 v[88:91], v[182:185], v[174:177], v[88:91]
	v_mfma_f32_16x16x32_f16 v[92:95], v[190:193], v[174:177], v[92:95]
	s_setprio 0
	s_barrier
	ds_read_b128 v[130:133], v224
	ds_read_b128 v[134:137], v224 offset:1024
	ds_read_b128 v[138:141], v224 offset:2048
	ds_read_b128 v[142:145], v224 offset:3072
	ds_read_b128 v[146:149], v225
	ds_read_b128 v[150:153], v225 offset:1024
	ds_read_b128 v[154:157], v226
	ds_read_b128 v[158:161], v226 offset:1024
	ds_read_b128 v[162:165], v227
	ds_read_b128 v[166:169], v227 offset:1024
	ds_read_b128 v[170:173], v228
	ds_read_b128 v[174:177], v228 offset:1024
	s_setprio 2
	v_readlane_b32 s12, v248, s9
	s_mov_b32 m0, s27
	s_nop 1
	v_add_u32_e32 v178, s12, v249
	global_load_lds_dwordx4 v178, s[18:19]
	v_add_u32_e32 v178, s12, v250
	s_mov_b32 m0, s28
	s_nop 0
	global_load_lds_dwordx4 v178, s[18:19]
	s_setprio 0
	s_waitcnt vmcnt(10)
	s_waitcnt lgkmcnt(8)
	s_barrier
	s_waitcnt lgkmcnt(0)
	s_setprio 1
	s_waitcnt lgkmcnt(0)
	v_mfma_f32_16x16x32_f16 v[124:127], v[130:133], v[146:149], v[124:127]
	v_mfma_f32_16x16x32_f16 v[120:123], v[138:141], v[146:149], v[120:123]
	v_mfma_f32_16x16x32_f16 v[116:119], v[130:133], v[154:157], v[116:119]
	v_mfma_f32_16x16x32_f16 v[112:115], v[138:141], v[154:157], v[112:115]
	v_mfma_f32_16x16x32_f16 v[108:111], v[130:133], v[162:165], v[108:111]
	v_mfma_f32_16x16x32_f16 v[104:107], v[138:141], v[162:165], v[104:107]
	v_mfma_f32_16x16x32_f16 v[100:103], v[130:133], v[170:173], v[100:103]
	v_mfma_f32_16x16x32_f16 v[96:99], v[138:141], v[170:173], v[96:99]
	v_mfma_f32_16x16x32_f16 v[124:127], v[134:137], v[150:153], v[124:127]
	v_mfma_f32_16x16x32_f16 v[120:123], v[142:145], v[150:153], v[120:123]
	v_mfma_f32_16x16x32_f16 v[116:119], v[134:137], v[158:161], v[116:119]
	v_mfma_f32_16x16x32_f16 v[112:115], v[142:145], v[158:161], v[112:115]
	v_mfma_f32_16x16x32_f16 v[108:111], v[134:137], v[166:169], v[108:111]
	v_mfma_f32_16x16x32_f16 v[104:107], v[142:145], v[166:169], v[104:107]
	v_mfma_f32_16x16x32_f16 v[100:103], v[134:137], v[174:177], v[100:103]
	v_mfma_f32_16x16x32_f16 v[96:99], v[142:145], v[174:177], v[96:99]
	s_setprio 0
	s_barrier
	ds_read_b128 v[178:181], v229
	ds_read_b128 v[182:185], v229 offset:1024
	ds_read_b128 v[186:189], v229 offset:2048
	ds_read_b128 v[190:193], v229 offset:3072
	s_setprio 2
	s_mov_b32 m0, s37
	v_add_u32_e32 v194, 0x48000, v129
	global_load_lds_dwordx4 v129, s[10:11]
	s_mov_b32 m0, s38
	s_add_i32 s12, s8, 3
	global_load_lds_dwordx4 v194, s[10:11]
	s_setprio 0
	s_waitcnt vmcnt(10)
	s_barrier
	s_waitcnt lgkmcnt(0)
	s_setprio 1
	s_waitcnt lgkmcnt(0)
	v_mfma_f32_16x16x32_f16 v[52:55], v[178:181], v[146:149], v[52:55]
	v_mfma_f32_16x16x32_f16 v[40:43], v[186:189], v[146:149], v[40:43]
	v_mfma_f32_16x16x32_f16 v[36:39], v[178:181], v[154:157], v[36:39]
	v_mfma_f32_16x16x32_f16 v[32:35], v[186:189], v[154:157], v[32:35]
	v_mfma_f32_16x16x32_f16 v[28:31], v[178:181], v[162:165], v[28:31]
	v_mfma_f32_16x16x32_f16 v[24:27], v[186:189], v[162:165], v[24:27]
	v_mfma_f32_16x16x32_f16 v[20:23], v[178:181], v[170:173], v[20:23]
	v_mfma_f32_16x16x32_f16 v[16:19], v[186:189], v[170:173], v[16:19]
	v_mfma_f32_16x16x32_f16 v[52:55], v[182:185], v[150:153], v[52:55]
	v_mfma_f32_16x16x32_f16 v[40:43], v[190:193], v[150:153], v[40:43]
	v_mfma_f32_16x16x32_f16 v[36:39], v[182:185], v[158:161], v[36:39]
	v_mfma_f32_16x16x32_f16 v[32:35], v[190:193], v[158:161], v[32:35]
	v_mfma_f32_16x16x32_f16 v[28:31], v[182:185], v[166:169], v[28:31]
	v_mfma_f32_16x16x32_f16 v[24:27], v[190:193], v[166:169], v[24:27]
	v_mfma_f32_16x16x32_f16 v[20:23], v[182:185], v[174:177], v[20:23]
	v_mfma_f32_16x16x32_f16 v[16:19], v[190:193], v[174:177], v[16:19]
	s_setprio 0
	s_barrier
	ds_read_b128 v[146:149], v230
	ds_read_b128 v[150:153], v230 offset:1024
	ds_read_b128 v[154:157], v231
	ds_read_b128 v[158:161], v231 offset:1024
	ds_read_b128 v[162:165], v232
	ds_read_b128 v[166:169], v232 offset:1024
	ds_read_b128 v[170:173], v233
	ds_read_b128 v[174:177], v233 offset:1024
	s_setprio 2
	v_readlane_b32 s13, v248, s12
	s_mov_b32 m0, s39
	s_nop 1
	v_add_u32_e32 v194, s13, v206
	global_load_lds_dwordx4 v194, s[18:19]
	v_add_u32_e32 v194, s13, v213
	s_mov_b32 m0, s40
	s_nop 0
	global_load_lds_dwordx4 v194, s[18:19]
	s_setprio 0
	s_barrier
	s_waitcnt lgkmcnt(0)
	s_setprio 1
	s_waitcnt lgkmcnt(0)
	v_mfma_f32_16x16x32_f16 v[12:15], v[130:133], v[146:149], v[12:15]
	v_mfma_f32_16x16x32_f16 v[8:11], v[138:141], v[146:149], v[8:11]
	v_mfma_f32_16x16x32_f16 v[4:7], v[130:133], v[154:157], v[4:7]
	v_mfma_f32_16x16x32_f16 v[0:3], v[138:141], v[154:157], v[0:3]
	v_mfma_f32_16x16x32_f16 v[44:47], v[130:133], v[162:165], v[44:47]
	v_mfma_f32_16x16x32_f16 v[48:51], v[138:141], v[162:165], v[48:51]
	v_mfma_f32_16x16x32_f16 v[56:59], v[130:133], v[170:173], v[56:59]
	v_mfma_f32_16x16x32_f16 v[60:63], v[138:141], v[170:173], v[60:63]
	v_mfma_f32_16x16x32_f16 v[12:15], v[134:137], v[150:153], v[12:15]
	v_mfma_f32_16x16x32_f16 v[8:11], v[142:145], v[150:153], v[8:11]
	v_mfma_f32_16x16x32_f16 v[4:7], v[134:137], v[158:161], v[4:7]
	v_mfma_f32_16x16x32_f16 v[0:3], v[142:145], v[158:161], v[0:3]
	v_mfma_f32_16x16x32_f16 v[44:47], v[134:137], v[166:169], v[44:47]
	v_mfma_f32_16x16x32_f16 v[48:51], v[142:145], v[166:169], v[48:51]
	v_mfma_f32_16x16x32_f16 v[56:59], v[134:137], v[174:177], v[56:59]
	v_mfma_f32_16x16x32_f16 v[60:63], v[142:145], v[174:177], v[60:63]
	s_setprio 0
	s_barrier
	s_setprio 2
	s_mov_b32 m0, s41
	v_add_u32_e32 v130, 0x90000, v129
	global_load_lds_dwordx4 v130, s[10:11]
	v_add_u32_e32 v129, 0xd8000, v129
	s_mov_b32 m0, s42
	s_nop 0
	global_load_lds_dwordx4 v129, s[10:11]
	s_setprio 0
	s_waitcnt vmcnt(10)
	s_barrier
	s_setprio 1
	v_mfma_f32_16x16x32_f16 v[64:67], v[178:181], v[146:149], v[64:67]
	v_mfma_f32_16x16x32_f16 v[68:71], v[186:189], v[146:149], v[68:71]
	v_mfma_f32_16x16x32_f16 v[72:75], v[178:181], v[154:157], v[72:75]
	v_mfma_f32_16x16x32_f16 v[76:79], v[186:189], v[154:157], v[76:79]
	v_mfma_f32_16x16x32_f16 v[80:83], v[178:181], v[162:165], v[80:83]
	v_mfma_f32_16x16x32_f16 v[84:87], v[186:189], v[162:165], v[84:87]
	v_mfma_f32_16x16x32_f16 v[88:91], v[178:181], v[170:173], v[88:91]
	v_mfma_f32_16x16x32_f16 v[92:95], v[186:189], v[170:173], v[92:95]
	v_mfma_f32_16x16x32_f16 v[64:67], v[182:185], v[150:153], v[64:67]
	v_mfma_f32_16x16x32_f16 v[68:71], v[190:193], v[150:153], v[68:71]
	v_mfma_f32_16x16x32_f16 v[72:75], v[182:185], v[158:161], v[72:75]
	v_mfma_f32_16x16x32_f16 v[76:79], v[190:193], v[158:161], v[76:79]
	v_mfma_f32_16x16x32_f16 v[80:83], v[182:185], v[166:169], v[80:83]
	v_mfma_f32_16x16x32_f16 v[84:87], v[190:193], v[166:169], v[84:87]
	v_mfma_f32_16x16x32_f16 v[88:91], v[182:185], v[174:177], v[88:91]
	v_mfma_f32_16x16x32_f16 v[92:95], v[190:193], v[174:177], v[92:95]
	s_setprio 0
	s_addk_i32 s7, 0x100
	s_cmp_lt_u32 s8, 32
	s_mov_b32 s8, s9
	s_barrier
	s_cbranch_scc1 .LBB1_82
	ds_read_b128 v[132:135], v219 offset:32768
	ds_read_b128 v[136:139], v219 offset:33792
	ds_read_b128 v[140:143], v219 offset:34816
	ds_read_b128 v[144:147], v219 offset:35840
	ds_read_b128 v[128:131], v220
	ds_read_b128 v[148:151], v220 offset:1024
	ds_read_b128 v[152:155], v221
	ds_read_b128 v[156:159], v221 offset:1024
	ds_read_b128 v[188:191], v222
	ds_read_b128 v[192:195], v222 offset:1024
	ds_read_b128 v[196:199], v223
	ds_read_b128 v[200:203], v223 offset:1024
	s_setprio 2
	s_lshl_b32 s3, s50, 9
	s_add_i32 s3, s47, s3
	s_add_i32 s3, s3, 0x10380
	s_mov_b32 m0, s43
	v_add_u32_e32 v160, s3, v206
	global_load_lds_dwordx4 v160, s[18:19]
	v_add_u32_e32 v160, s3, v213
	s_mov_b32 m0, s44
	s_nop 0
	global_load_lds_dwordx4 v160, s[18:19]
	s_setprio 0
	s_waitcnt vmcnt(10)
	s_barrier
	s_waitcnt lgkmcnt(0)
	s_setprio 1
	s_waitcnt lgkmcnt(0)
	v_mfma_f32_16x16x32_f16 v[124:127], v[132:135], v[128:131], v[124:127]
	v_mfma_f32_16x16x32_f16 v[120:123], v[140:143], v[128:131], v[120:123]
	v_mfma_f32_16x16x32_f16 v[116:119], v[132:135], v[152:155], v[116:119]
	v_mfma_f32_16x16x32_f16 v[112:115], v[140:143], v[152:155], v[112:115]
	v_mfma_f32_16x16x32_f16 v[108:111], v[132:135], v[188:191], v[108:111]
	v_mfma_f32_16x16x32_f16 v[104:107], v[140:143], v[188:191], v[104:107]
	v_mfma_f32_16x16x32_f16 v[100:103], v[132:135], v[196:199], v[100:103]
	v_mfma_f32_16x16x32_f16 v[96:99], v[140:143], v[196:199], v[96:99]
	v_mfma_f32_16x16x32_f16 v[160:163], v[136:139], v[148:151], v[124:127]
	v_mfma_f32_16x16x32_f16 v[164:167], v[144:147], v[148:151], v[120:123]
	v_mfma_f32_16x16x32_f16 v[168:171], v[136:139], v[156:159], v[116:119]
	v_mfma_f32_16x16x32_f16 v[172:175], v[144:147], v[156:159], v[112:115]
	v_mfma_f32_16x16x32_f16 v[176:179], v[136:139], v[192:195], v[108:111]
	v_mfma_f32_16x16x32_f16 v[180:183], v[144:147], v[192:195], v[104:107]
	v_mfma_f32_16x16x32_f16 v[100:103], v[136:139], v[200:203], v[100:103]
	v_mfma_f32_16x16x32_f16 v[184:187], v[144:147], v[200:203], v[96:99]
	s_setprio 0
	s_barrier
	ds_read_b128 v[104:107], v219 offset:49152
	ds_read_b128 v[108:111], v219 offset:50176
	ds_read_b128 v[116:119], v219 offset:51200
	ds_read_b128 v[236:239], v219 offset:52224
	s_waitcnt vmcnt(8)
	s_barrier
	s_waitcnt lgkmcnt(0)
	s_setprio 1
	s_waitcnt lgkmcnt(0)
	v_mfma_f32_16x16x32_f16 v[52:55], v[104:107], v[128:131], v[52:55]
	v_mfma_f32_16x16x32_f16 v[40:43], v[116:119], v[128:131], v[40:43]
	v_mfma_f32_16x16x32_f16 v[36:39], v[104:107], v[152:155], v[36:39]
	v_mfma_f32_16x16x32_f16 v[32:35], v[116:119], v[152:155], v[32:35]
	v_mfma_f32_16x16x32_f16 v[28:31], v[104:107], v[188:191], v[28:31]
	v_mfma_f32_16x16x32_f16 v[24:27], v[116:119], v[188:191], v[24:27]
	v_mfma_f32_16x16x32_f16 v[20:23], v[104:107], v[196:199], v[20:23]
	v_mfma_f32_16x16x32_f16 v[16:19], v[116:119], v[196:199], v[16:19]
	v_mfma_f32_16x16x32_f16 v[52:55], v[108:111], v[148:151], v[52:55]
	v_mfma_f32_16x16x32_f16 v[40:43], v[236:239], v[148:151], v[40:43]
	v_mfma_f32_16x16x32_f16 v[36:39], v[108:111], v[156:159], v[36:39]
	v_mfma_f32_16x16x32_f16 v[32:35], v[236:239], v[156:159], v[32:35]
	v_mfma_f32_16x16x32_f16 v[28:31], v[108:111], v[192:195], v[28:31]
	v_mfma_f32_16x16x32_f16 v[24:27], v[236:239], v[192:195], v[24:27]
	v_mfma_f32_16x16x32_f16 v[96:99], v[108:111], v[200:203], v[20:23]
	v_mfma_f32_16x16x32_f16 v[16:19], v[236:239], v[200:203], v[16:19]
	s_setprio 0
	s_barrier
	ds_read_b128 v[20:23], v220 offset:16384
	ds_read_b128 v[148:151], v220 offset:17408
	ds_read_b128 v[152:155], v221 offset:16384
	ds_read_b128 v[156:159], v221 offset:17408
	ds_read_b128 v[188:191], v222 offset:16384
	ds_read_b128 v[192:195], v222 offset:17408
	ds_read_b128 v[196:199], v223 offset:16384
	ds_read_b128 v[200:203], v223 offset:17408
	s_waitcnt vmcnt(4)
	s_barrier
	s_waitcnt lgkmcnt(0)
	s_setprio 1
	s_waitcnt lgkmcnt(0)
	v_mfma_f32_16x16x32_f16 v[0:3], v[140:143], v[152:155], v[0:3]
	v_mfma_f32_16x16x32_f16 v[124:127], v[144:147], v[156:159], v[0:3]
	v_mfma_f32_16x16x32_f16 v[0:3], v[132:135], v[188:191], v[44:47]
	v_mfma_f32_16x16x32_f16 v[128:131], v[136:139], v[192:195], v[0:3]
	v_mfma_f32_16x16x32_f16 v[0:3], v[140:143], v[188:191], v[48:51]
	v_mfma_f32_16x16x32_f16 v[48:51], v[144:147], v[192:195], v[0:3]
	v_mfma_f32_16x16x32_f16 v[0:3], v[132:135], v[196:199], v[56:59]
	v_mfma_f32_16x16x32_f16 v[12:15], v[132:135], v[20:23], v[12:15]
	v_mfma_f32_16x16x32_f16 v[8:11], v[140:143], v[20:23], v[8:11]
	v_mfma_f32_16x16x32_f16 v[4:7], v[132:135], v[152:155], v[4:7]
	v_mfma_f32_16x16x32_f16 v[56:59], v[136:139], v[200:203], v[0:3]
	v_mfma_f32_16x16x32_f16 v[0:3], v[140:143], v[196:199], v[60:63]
	v_mfma_f32_16x16x32_f16 v[112:115], v[136:139], v[148:151], v[12:15]
	v_mfma_f32_16x16x32_f16 v[8:11], v[144:147], v[148:151], v[8:11]
	v_mfma_f32_16x16x32_f16 v[120:123], v[136:139], v[156:159], v[4:7]
	v_mfma_f32_16x16x32_f16 v[60:63], v[144:147], v[200:203], v[0:3]
	s_setprio 0
	s_setprio 1
	v_mfma_f32_16x16x32_f16 v[0:3], v[104:107], v[20:23], v[64:67]
	v_mfma_f32_16x16x32_f16 v[132:135], v[108:111], v[148:151], v[0:3]
	v_mfma_f32_16x16x32_f16 v[0:3], v[116:119], v[20:23], v[68:71]
	v_mfma_f32_16x16x32_f16 v[136:139], v[236:239], v[148:151], v[0:3]
	v_mfma_f32_16x16x32_f16 v[0:3], v[104:107], v[152:155], v[72:75]
	v_mfma_f32_16x16x32_f16 v[140:143], v[108:111], v[156:159], v[0:3]
	v_mfma_f32_16x16x32_f16 v[0:3], v[116:119], v[152:155], v[76:79]
	v_mfma_f32_16x16x32_f16 v[144:147], v[236:239], v[156:159], v[0:3]
	v_mfma_f32_16x16x32_f16 v[0:3], v[104:107], v[188:191], v[80:83]
	v_mfma_f32_16x16x32_f16 v[80:83], v[108:111], v[192:195], v[0:3]
	v_mfma_f32_16x16x32_f16 v[0:3], v[116:119], v[188:191], v[84:87]
	v_mfma_f32_16x16x32_f16 v[148:151], v[236:239], v[192:195], v[0:3]
	v_mfma_f32_16x16x32_f16 v[0:3], v[104:107], v[196:199], v[88:91]
	v_mfma_f32_16x16x32_f16 v[152:155], v[108:111], v[200:203], v[0:3]
	v_mfma_f32_16x16x32_f16 v[0:3], v[116:119], v[196:199], v[92:95]
	v_mfma_f32_16x16x32_f16 v[156:159], v[236:239], v[200:203], v[0:3]
	s_setprio 0
	s_add_i32 s49, s49, s17
	s_cmpk_lt_i32 s49, 0x1c8
	s_cselect_b64 s[6:7], -1, 0
	s_cmpk_gt_i32 s49, 0x1c7
	s_cselect_b64 s[12:13], -1, 0
	s_and_b64 vcc, exec, s[12:13]
	s_mov_b32 s54, s2
	s_mov_b32 s53, s51
	s_mov_b32 s55, s52
	s_barrier
	s_cbranch_vccnz .LBB1_100
	s_cmpk_lt_i32 s49, 0x148
	s_cbranch_scc1 .LBB1_88
	s_cmpk_lt_u32 s49, 0x1a0
	s_cbranch_scc1 .LBB1_89
	s_cmpk_lt_u32 s49, 0x1b8
	s_cbranch_scc1 .LBB1_90
	s_cmpk_lt_u32 s49, 0x1c0
	s_cselect_b32 s47, s45, 0xfffffe40
	s_cselect_b32 s48, 3, 4
	s_mov_b32 s3, 1
	s_cmp_lt_i32 s48, 1
	s_movk_i32 s53, 0x64
	s_cbranch_scc0 .LBB1_91
	s_branch .LBB1_99
